# speedup vs baseline: 1.0209x; 1.0083x over previous
.LBB0_18:
	v_mfma_f32_32x32x16_bf16 a[48:63], v[60:63], v[140:143], a[48:63]
	v_cvt_pk_bf16_f32 v156, v227, v228
	v_cvt_pk_bf16_f32 v157, v229, v230
	v_cvt_pk_bf16_f32 v158, v231, v232
	v_cvt_pk_bf16_f32 v159, v233, v234
	v_cvt_pk_bf16_f32 v160, v148, v149
	v_cvt_pk_bf16_f32 v161, v150, v151
	v_cvt_pk_bf16_f32 v162, v152, v153
	v_cvt_pk_bf16_f32 v163, v154, v155
	v_mfma_f32_32x32x16_bf16 a[64:79], v[56:59], v[52:55], a[64:79]
	v_exp_f32_e32 v128, v112
	v_exp_f32_e32 v129, v113
	v_exp_f32_e32 v130, v114
	v_exp_f32_e32 v131, v115
	v_mfma_f32_32x32x16_bf16 a[80:95], v[56:59], v[140:143], a[80:95]
	v_exp_f32_e32 v132, v116
	v_exp_f32_e32 v133, v117
	v_exp_f32_e32 v134, v118
	v_add_f32_e32 v56, v128, v130
	v_add_f32_e32 v57, v129, v131
	v_mfma_f32_32x32x16_bf16 a[96:111], v[48:51], v[52:55], a[96:111]
	v_exp_f32_e32 v135, v119
	v_exp_f32_e32 v136, v120
	v_add_f32_e32 v52, v56, v132
	v_add_f32_e32 v53, v57, v133
	v_add_f32_e32 v52, v52, v134
	v_exp_f32_e32 v137, v121
	v_mfma_f32_32x32x16_bf16 a[112:127], v[48:51], v[140:143], a[112:127]
	v_exp_f32_e32 v138, v122
	v_exp_f32_e32 v139, v123
	v_add_f32_e32 v48, v53, v135
	v_add_f32_e32 v49, v52, v136
	v_exp_f32_e32 v140, v124
	v_mfma_f32_32x32x16_bf16 a[0:15], v[44:47], v[156:159], a[0:15]
	v_exp_f32_e32 v141, v125
	v_add_f32_e32 v48, v48, v137
	v_add_f32_e32 v49, v49, v138
	v_add_f32_e32 v48, v48, v139
	v_exp_f32_e32 v142, v126
	v_exp_f32_e32 v143, v127
	v_mfma_f32_32x32x16_bf16 a[16:31], v[44:47], v[160:163], a[16:31]
	v_exp_f32_e32 v144, v96
	v_add_f32_e32 v44, v49, v140
	v_add_f32_e32 v45, v48, v141
	v_exp_f32_e32 v145, v97
	v_exp_f32_e32 v146, v98
	v_mfma_f32_32x32x16_bf16 a[32:47], v[40:43], v[156:159], a[32:47]
	v_add_f32_e32 v236, v44, v142
	v_add_f32_e32 v235, v45, v143
	v_exp_f32_e32 v147, v99
	v_exp_f32_e32 v148, v100
	v_exp_f32_e32 v149, v101
	v_mfma_f32_32x32x16_bf16 a[48:63], v[40:43], v[160:163], a[48:63]
	v_add_f32_e32 v41, v144, v146
	v_exp_f32_e32 v150, v102
	v_exp_f32_e32 v151, v103
	v_add_f32_e32 v40, v145, v147
	v_add_f32_e32 v41, v41, v148
	v_add_f32_e32 v40, v40, v149
	v_mfma_f32_32x32x16_bf16 a[64:79], v[36:39], v[156:159], a[64:79]
	v_exp_f32_e32 v152, v104
	v_exp_f32_e32 v153, v105
	v_exp_f32_e32 v154, v106
	v_exp_f32_e32 v155, v107
	v_mfma_f32_32x32x16_bf16 a[80:95], v[36:39], v[160:163], a[80:95]
	v_add_f32_e32 v36, v41, v150
	v_add_f32_e32 v37, v40, v151
	v_add_f32_e32 v36, v36, v152
	v_add_f32_e32 v37, v37, v153
	v_add_f32_e32 v36, v36, v154
	v_mfma_f32_32x32x16_bf16 a[96:111], v[32:35], v[156:159], a[96:111]
	v_exp_f32_e32 v156, v108
	v_exp_f32_e32 v157, v109
	v_exp_f32_e32 v158, v110
	v_exp_f32_e32 v159, v111
	v_mfma_f32_32x32x16_bf16 a[112:127], v[32:35], v[160:163], a[112:127]
	v_add_f32_e32 v32, v37, v155
	v_add_f32_e32 v33, v36, v156
	s_andn2_b64 vcc, exec, s[0:1]
	v_add_f32_e32 v32, v32, v157
	v_add_f32_e32 v237, v33, v158
	s_nop 0
	v_add_f32_e32 v238, v32, v159
	s_cbranch_vccz .LBB0_23

.LBB0_20:
	v_mfma_f32_32x32x16_bf16 a[48:63], v[92:95], v[140:143], a[48:63]
	v_cvt_pk_bf16_f32 v156, v227, v228
	v_cvt_pk_bf16_f32 v157, v229, v230
	v_cvt_pk_bf16_f32 v158, v231, v232
	v_cvt_pk_bf16_f32 v159, v233, v234
	v_cvt_pk_bf16_f32 v160, v148, v149
	v_cvt_pk_bf16_f32 v161, v150, v151
	v_cvt_pk_bf16_f32 v162, v152, v153
	v_cvt_pk_bf16_f32 v163, v154, v155
	v_mfma_f32_32x32x16_bf16 a[64:79], v[88:91], v[84:87], a[64:79]
	v_exp_f32_e32 v128, v112
	v_exp_f32_e32 v129, v113
	v_exp_f32_e32 v130, v114
	v_exp_f32_e32 v131, v115
	v_mfma_f32_32x32x16_bf16 a[80:95], v[88:91], v[140:143], a[80:95]
	v_exp_f32_e32 v132, v116
	v_exp_f32_e32 v133, v117
	v_exp_f32_e32 v134, v118
	v_add_f32_e32 v88, v128, v130
	v_add_f32_e32 v89, v129, v131
	v_mfma_f32_32x32x16_bf16 a[96:111], v[80:83], v[84:87], a[96:111]
	v_exp_f32_e32 v135, v119
	v_exp_f32_e32 v136, v120
	v_add_f32_e32 v84, v88, v132
	v_add_f32_e32 v85, v89, v133
	v_add_f32_e32 v84, v84, v134
	v_exp_f32_e32 v137, v121
	v_mfma_f32_32x32x16_bf16 a[112:127], v[80:83], v[140:143], a[112:127]
	v_exp_f32_e32 v138, v122
	v_exp_f32_e32 v139, v123
	v_add_f32_e32 v80, v85, v135
	v_add_f32_e32 v81, v84, v136
	v_exp_f32_e32 v140, v124
	v_mfma_f32_32x32x16_bf16 a[0:15], v[76:79], v[156:159], a[0:15]
	v_exp_f32_e32 v141, v125
	v_add_f32_e32 v80, v80, v137
	v_add_f32_e32 v81, v81, v138
	v_add_f32_e32 v80, v80, v139
	v_exp_f32_e32 v142, v126
	v_exp_f32_e32 v143, v127
	v_mfma_f32_32x32x16_bf16 a[16:31], v[76:79], v[160:163], a[16:31]
	v_exp_f32_e32 v144, v96
	v_add_f32_e32 v76, v81, v140
	v_add_f32_e32 v77, v80, v141
	v_exp_f32_e32 v145, v97
	v_exp_f32_e32 v146, v98
	v_mfma_f32_32x32x16_bf16 a[32:47], v[72:75], v[156:159], a[32:47]
	v_add_f32_e32 v236, v76, v142
	v_add_f32_e32 v235, v77, v143
	v_exp_f32_e32 v147, v99
	v_exp_f32_e32 v148, v100
	v_exp_f32_e32 v149, v101
	v_mfma_f32_32x32x16_bf16 a[48:63], v[72:75], v[160:163], a[48:63]
	v_add_f32_e32 v73, v144, v146
	v_exp_f32_e32 v150, v102
	v_exp_f32_e32 v151, v103
	v_add_f32_e32 v72, v145, v147
	v_add_f32_e32 v73, v73, v148
	v_add_f32_e32 v72, v72, v149
	v_mfma_f32_32x32x16_bf16 a[64:79], v[68:71], v[156:159], a[64:79]
	v_exp_f32_e32 v152, v104
	v_exp_f32_e32 v153, v105
	v_exp_f32_e32 v154, v106
	v_exp_f32_e32 v155, v107
	v_mfma_f32_32x32x16_bf16 a[80:95], v[68:71], v[160:163], a[80:95]
	v_add_f32_e32 v68, v73, v150
	v_add_f32_e32 v69, v72, v151
	v_add_f32_e32 v68, v68, v152
	v_add_f32_e32 v69, v69, v153
	v_add_f32_e32 v68, v68, v154
	v_mfma_f32_32x32x16_bf16 a[96:111], v[64:67], v[156:159], a[96:111]
	v_exp_f32_e32 v156, v108
	v_exp_f32_e32 v157, v109
	v_exp_f32_e32 v158, v110
	v_exp_f32_e32 v159, v111
	v_mfma_f32_32x32x16_bf16 a[112:127], v[64:67], v[160:163], a[112:127]
	v_add_f32_e32 v64, v69, v155
	v_add_f32_e32 v65, v68, v156
	s_andn2_b64 vcc, exec, s[0:1]
	v_add_f32_e32 v64, v64, v157
	v_add_f32_e32 v237, v65, v158
	s_nop 0
	v_add_f32_e32 v238, v64, v159
	s_cbranch_vccz .LBB0_25
